# speedup vs baseline: 1.0209x; 1.0209x over previous
_Z9k_gemm_tlILi3ELb0EEvPKDF16_6TlArgs:
	s_load_dwordx4 s[8:11], s[0:1], 0x0
	s_load_dwordx4 s[4:7], s[0:1], 0x30
	v_lshrrev_b32_e32 v43, 6, v0
	s_lshl_b32 s1, s2, 6
	v_lshl_or_b32 v34, s3, 2, v43
	v_mov_b32_e32 v35, 0
	s_lshr_b32 s0, s2, 6
	s_and_b32 s2, s1, 0xfc0
	s_mov_b32 s1, 0
	v_lshlrev_b64 v[2:3], 15, v[34:35]
	s_waitcnt lgkmcnt(0)
	s_lshl_b32 s12, s3, 7
	v_lshrrev_b32_e32 v126, 4, v0
	v_or_b32_e32 v126, s12, v126
	v_lshlrev_b32_e32 v126, 2, v126
	global_load_dword v110, v126, s[4:5]
	global_load_dword v112, v126, s[4:5] offset:64
	global_load_dword v114, v126, s[4:5] offset:128
	global_load_dword v116, v126, s[4:5] offset:192
	global_load_dword v118, v126, s[4:5] offset:256
	global_load_dword v120, v126, s[4:5] offset:320
	global_load_dword v122, v126, s[4:5] offset:384
	global_load_dword v124, v126, s[4:5] offset:448
	v_lshl_add_u64 v[2:3], s[8:9], 0, v[2:3]
	s_lshl_b64 s[8:9], s[0:1], 22
	s_add_u32 s8, s10, s8
	v_lshlrev_b32_e32 v42, 4, v0
	s_addc_u32 s9, s11, s9
	s_lshl_b32 s10, s2, 1
	v_and_b32_e32 v34, 0x3f0, v42
	s_add_u32 s8, s8, s10
	v_lshl_add_u64 v[36:37], v[2:3], 0, v[34:35]
	v_lshrrev_b32_e32 v44, 3, v0
	s_addc_u32 s9, s9, 0
	v_and_b32_e32 v34, 0x70, v42
	v_or_b32_e32 v1, 0x100, v0
	v_lshl_add_u64 v[2:3], s[8:9], 0, v[34:35]
	v_lshrrev_b32_e32 v14, 3, v1
	v_lshlrev_b32_e32 v4, 13, v44
	v_mov_b32_e32 v5, v35
	v_lshl_add_u64 v[38:39], v[2:3], 0, v[4:5]
	v_lshlrev_b32_e32 v4, 13, v14
	v_lshl_add_u64 v[40:41], v[2:3], 0, v[4:5]
	global_load_dwordx4 v[2:5], v[38:39], off
	global_load_dwordx4 v[6:9], v[40:41], off
	global_load_dwordx4 v[18:21], v[36:37], off
	global_load_dwordx4 v[48:51], v[36:37], off offset:1024
	global_load_dwordx4 v[52:55], v[36:37], off offset:2048
	global_load_dwordx4 v[56:59], v[36:37], off offset:3072
	v_lshrrev_b32_e32 v11, 2, v0
	v_lshlrev_b32_e32 v10, 3, v0
	v_and_b32_e32 v12, 16, v0
	v_and_b32_e32 v11, 11, v11
	s_movk_i32 s8, 0x1000
	v_and_b32_e32 v10, 24, v10
	v_lshlrev_b32_e32 v12, 1, v12
	v_mul_u32_u24_e32 v11, 0x90, v11
	v_add3_u32 v45, v11, v10, v12
	v_add_co_u32_e32 v10, vcc, s8, v36
	s_mov_b32 s10, 0x80000
	s_nop 0
	v_addc_co_u32_e32 v11, vcc, 0, v37, vcc
	v_add_co_u32_e32 v12, vcc, s10, v38
	s_movk_i32 s9, 0x2000
	s_nop 0
	v_addc_co_u32_e32 v13, vcc, 0, v39, vcc
	global_load_dwordx4 v[60:63], v[12:13], off
	v_add_co_u32_e32 v12, vcc, s10, v40
	s_movk_i32 s11, 0x90
	s_nop 0
	v_addc_co_u32_e32 v13, vcc, 0, v41, vcc
	v_add_co_u32_e32 v104, vcc, s9, v36
	global_load_dwordx4 v[64:67], v[12:13], off
	s_nop 0
	v_addc_co_u32_e32 v105, vcc, 0, v37, vcc
	global_load_dwordx4 v[68:71], v[104:105], off offset:-4096
	global_load_dwordx4 v[72:75], v[10:11], off offset:1024
	global_load_dwordx4 v[76:79], v[10:11], off offset:2048
	global_load_dwordx4 v[80:83], v[10:11], off offset:3072
	v_mad_u32_u24 v46, v44, s11, v34
	v_mad_u32_u24 v34, v14, s11, v34
	s_mov_b32 s8, 0x100000
	v_add_co_u32_e32 v106, vcc, s8, v38
	s_mov_b32 s9, 0x180000
	s_nop 0
	v_addc_co_u32_e32 v107, vcc, 0, v39, vcc
	v_add_co_u32_e32 v108, vcc, s8, v40
	s_movk_i32 s8, 0x3000
	s_nop 0
	v_addc_co_u32_e32 v109, vcc, 0, v41, vcc
	s_lshl_b32 s3, s3, 7
	s_lshl_b64 s[0:1], s[0:1], 23
	s_add_u32 s0, s6, s0
	s_addc_u32 s1, s7, s1
	s_lshl_b32 s2, s2, 2
	s_add_u32 s0, s0, s2
	s_addc_u32 s1, s1, 0
	v_lshrrev_b32_e32 v1, 4, v1
	s_waitcnt vmcnt(11)
	ds_write_b128 v46, v[2:5]
	s_waitcnt vmcnt(10)
	ds_write_b128 v34, v[6:9]
	s_waitcnt lgkmcnt(0)
	s_barrier
	ds_read_b64_tr_b16 v[2:3], v45
	ds_read_b64_tr_b16 v[4:5], v45 offset:576
	ds_read_b64_tr_b16 v[24:25], v45 offset:640
	ds_read_b64_tr_b16 v[22:23], v45 offset:64
	s_waitcnt vmcnt(9) lgkmcnt(2)
	v_mfma_f32_32x32x16_f16 v[2:17], v[18:21], v[2:5], 0
	ds_read_b64_tr_b16 v[84:85], v45 offset:2304
	ds_read_b64_tr_b16 v[86:87], v45 offset:2880
	ds_read_b64_tr_b16 v[90:91], v45 offset:2944
	ds_read_b64_tr_b16 v[88:89], v45 offset:2368
	s_waitcnt lgkmcnt(4)
	v_mfma_f32_32x32x16_f16 v[18:33], v[18:21], v[22:25], 0
	s_waitcnt vmcnt(8) lgkmcnt(2)
	v_mfma_f32_32x32x16_f16 v[2:17], v[48:51], v[84:87], v[2:17]
	s_waitcnt lgkmcnt(0)
	v_mfma_f32_32x32x16_f16 v[18:33], v[48:51], v[88:91], v[18:33]
	ds_read_b64_tr_b16 v[48:49], v45 offset:4608
	ds_read_b64_tr_b16 v[50:51], v45 offset:5184
	ds_read_b64_tr_b16 v[86:87], v45 offset:5248
	ds_read_b64_tr_b16 v[84:85], v45 offset:4672
	s_waitcnt vmcnt(7) lgkmcnt(2)
	v_mfma_f32_32x32x16_f16 v[2:17], v[52:55], v[48:51], v[2:17]
	ds_read_b64_tr_b16 v[48:49], v45 offset:6912
	ds_read_b64_tr_b16 v[50:51], v45 offset:7488
	s_waitcnt lgkmcnt(2)
	v_mfma_f32_32x32x16_f16 v[18:33], v[52:55], v[84:87], v[18:33]
	ds_read_b64_tr_b16 v[54:55], v45 offset:7552
	ds_read_b64_tr_b16 v[52:53], v45 offset:6976
	s_waitcnt vmcnt(6) lgkmcnt(2)
	v_mfma_f32_32x32x16_f16 v[2:17], v[56:59], v[48:51], v[2:17]
	global_load_dwordx4 v[48:51], v[104:105], off
	global_load_dwordx4 v[84:87], v[104:105], off offset:1024
	global_load_dwordx4 v[88:91], v[106:107], off
	global_load_dwordx4 v[92:95], v[108:109], off
	global_load_dwordx4 v[96:99], v[104:105], off offset:2048
	global_load_dwordx4 v[100:103], v[104:105], off offset:3072
	s_waitcnt vmcnt(11)
	ds_write_b128 v46, v[60:63] offset:9216
	s_waitcnt vmcnt(10)
	ds_write_b128 v34, v[64:67] offset:9216
	s_waitcnt lgkmcnt(0)
	s_barrier
	v_add_co_u32_e32 v104, vcc, s8, v36
	v_mfma_f32_32x32x16_f16 v[18:33], v[56:59], v[52:55], v[18:33]
	ds_read_b64_tr_b16 v[52:53], v45 offset:9216
	ds_read_b64_tr_b16 v[54:55], v45 offset:9792
	ds_read_b64_tr_b16 v[58:59], v45 offset:9856
	ds_read_b64_tr_b16 v[56:57], v45 offset:9280
	v_addc_co_u32_e32 v105, vcc, 0, v37, vcc
	v_add_co_u32_e32 v64, vcc, s9, v38
	s_movk_i32 s8, 0x4000
	s_nop 0
	v_addc_co_u32_e32 v65, vcc, 0, v39, vcc
	s_waitcnt vmcnt(9) lgkmcnt(2)
	v_mfma_f32_32x32x16_f16 v[2:17], v[68:71], v[52:55], v[2:17]
	v_add_co_u32_e32 v66, vcc, s9, v40
	s_mov_b32 s9, 0x280000
	s_nop 0
	v_addc_co_u32_e32 v67, vcc, 0, v41, vcc
	v_add_co_u32_e32 v106, vcc, s8, v36
	s_waitcnt lgkmcnt(0)
	v_mfma_f32_32x32x16_f16 v[18:33], v[68:71], v[56:59], v[18:33]
	ds_read_b64_tr_b16 v[52:53], v45 offset:11520
	ds_read_b64_tr_b16 v[54:55], v45 offset:12096
	ds_read_b64_tr_b16 v[58:59], v45 offset:12160
	ds_read_b64_tr_b16 v[56:57], v45 offset:11584
	v_addc_co_u32_e32 v107, vcc, 0, v37, vcc
	s_mov_b32 s8, 0x200000
	s_waitcnt vmcnt(8) lgkmcnt(2)
	v_mfma_f32_32x32x16_f16 v[2:17], v[72:75], v[52:55], v[2:17]
	ds_read_b64_tr_b16 v[52:53], v45 offset:13824
	ds_read_b64_tr_b16 v[54:55], v45 offset:14400
	s_waitcnt lgkmcnt(2)
	v_mfma_f32_32x32x16_f16 v[18:33], v[72:75], v[56:59], v[18:33]
	ds_read_b64_tr_b16 v[58:59], v45 offset:14464
	ds_read_b64_tr_b16 v[56:57], v45 offset:13888
	s_waitcnt vmcnt(7) lgkmcnt(2)
	v_mfma_f32_32x32x16_f16 v[2:17], v[76:79], v[52:55], v[2:17]
	ds_read_b64_tr_b16 v[52:53], v45 offset:16128
	ds_read_b64_tr_b16 v[54:55], v45 offset:16704
	s_waitcnt lgkmcnt(2)
	v_mfma_f32_32x32x16_f16 v[18:33], v[76:79], v[56:59], v[18:33]
	global_load_dwordx4 v[56:59], v[64:65], off
	global_load_dwordx4 v[60:63], v[66:67], off
	ds_read_b64_tr_b16 v[66:67], v45 offset:16768
	ds_read_b64_tr_b16 v[64:65], v45 offset:16192
	s_waitcnt vmcnt(8) lgkmcnt(2)
	v_mfma_f32_32x32x16_f16 v[2:17], v[80:83], v[52:55], v[2:17]
	global_load_dwordx4 v[52:55], v[106:107], off offset:-4096
	global_load_dwordx4 v[68:71], v[104:105], off offset:1024
	global_load_dwordx4 v[72:75], v[104:105], off offset:2048
	global_load_dwordx4 v[76:79], v[104:105], off offset:3072
	s_waitcnt vmcnt(9)
	ds_write_b128 v46, v[88:91]
	s_waitcnt vmcnt(8)
	ds_write_b128 v34, v[92:95]
	s_waitcnt lgkmcnt(2)
	v_mfma_f32_32x32x16_f16 v[18:33], v[80:83], v[64:67], v[18:33]
	s_waitcnt lgkmcnt(0)
	s_barrier
	ds_read_b64_tr_b16 v[64:65], v45
	ds_read_b64_tr_b16 v[66:67], v45 offset:576
	ds_read_b64_tr_b16 v[82:83], v45 offset:640
	ds_read_b64_tr_b16 v[80:81], v45 offset:64
	v_add_co_u32_e32 v104, vcc, s8, v38
	s_waitcnt lgkmcnt(2)
	v_mfma_f32_32x32x16_f16 v[2:17], v[48:51], v[64:67], v[2:17]
	v_addc_co_u32_e32 v105, vcc, 0, v39, vcc
	v_add_co_u32_e32 v108, vcc, s8, v40
	s_movk_i32 s8, 0x5000
	s_nop 0
	v_addc_co_u32_e32 v109, vcc, 0, v41, vcc
	s_waitcnt lgkmcnt(0)
	v_mfma_f32_32x32x16_f16 v[18:33], v[48:51], v[80:83], v[18:33]
	ds_read_b64_tr_b16 v[48:49], v45 offset:2304
	ds_read_b64_tr_b16 v[50:51], v45 offset:2880
	ds_read_b64_tr_b16 v[66:67], v45 offset:2944
	ds_read_b64_tr_b16 v[64:65], v45 offset:2368
	s_waitcnt lgkmcnt(2)
	v_mfma_f32_32x32x16_f16 v[2:17], v[84:87], v[48:51], v[2:17]
	s_waitcnt lgkmcnt(0)
	v_mfma_f32_32x32x16_f16 v[18:33], v[84:87], v[64:67], v[18:33]
	ds_read_b64_tr_b16 v[48:49], v45 offset:4608
	ds_read_b64_tr_b16 v[50:51], v45 offset:5184
	ds_read_b64_tr_b16 v[66:67], v45 offset:5248
	ds_read_b64_tr_b16 v[64:65], v45 offset:4672
	s_waitcnt vmcnt(7) lgkmcnt(2)
	v_mfma_f32_32x32x16_f16 v[2:17], v[96:99], v[48:51], v[2:17]
	global_load_dwordx4 v[48:51], v[106:107], off
	global_load_dwordx4 v[80:83], v[106:107], off offset:1024
	s_waitcnt lgkmcnt(0)
	v_mfma_f32_32x32x16_f16 v[18:33], v[96:99], v[64:67], v[18:33]
	ds_read_b64_tr_b16 v[64:65], v45 offset:6912
	ds_read_b64_tr_b16 v[66:67], v45 offset:7488
	ds_read_b64_tr_b16 v[86:87], v45 offset:7552
	ds_read_b64_tr_b16 v[84:85], v45 offset:6976
	s_waitcnt vmcnt(8) lgkmcnt(2)
	v_mfma_f32_32x32x16_f16 v[2:17], v[100:103], v[64:67], v[2:17]
	global_load_dwordx4 v[64:67], v[104:105], off
	global_load_dwordx4 v[88:91], v[108:109], off
	global_load_dwordx4 v[92:95], v[106:107], off offset:2048
	global_load_dwordx4 v[96:99], v[106:107], off offset:3072
	s_waitcnt vmcnt(11)
	ds_write_b128 v46, v[56:59] offset:9216
	s_waitcnt vmcnt(10)
	ds_write_b128 v34, v[60:63] offset:9216
	s_waitcnt lgkmcnt(0)
	s_barrier
	ds_read_b64_tr_b16 v[56:57], v45 offset:9216
	ds_read_b64_tr_b16 v[58:59], v45 offset:9792
	ds_read_b64_tr_b16 v[62:63], v45 offset:9856
	ds_read_b64_tr_b16 v[60:61], v45 offset:9280
	v_mfma_f32_32x32x16_f16 v[18:33], v[100:103], v[84:87], v[18:33]
	v_add_co_u32_e32 v104, vcc, s8, v36
	s_movk_i32 s8, 0x6000
	s_nop 0
	v_addc_co_u32_e32 v105, vcc, 0, v37, vcc
	s_waitcnt vmcnt(9) lgkmcnt(2)
	v_mfma_f32_32x32x16_f16 v[2:17], v[52:55], v[56:59], v[2:17]
	s_waitcnt lgkmcnt(0)
	v_mfma_f32_32x32x16_f16 v[18:33], v[52:55], v[60:63], v[18:33]
	ds_read_b64_tr_b16 v[52:53], v45 offset:11520
	ds_read_b64_tr_b16 v[54:55], v45 offset:12096
	ds_read_b64_tr_b16 v[58:59], v45 offset:12160
	ds_read_b64_tr_b16 v[56:57], v45 offset:11584
	s_waitcnt vmcnt(8) lgkmcnt(2)
	v_mfma_f32_32x32x16_f16 v[2:17], v[68:71], v[52:55], v[2:17]
	ds_read_b64_tr_b16 v[52:53], v45 offset:13824
	ds_read_b64_tr_b16 v[54:55], v45 offset:14400
	s_waitcnt lgkmcnt(2)
	v_mfma_f32_32x32x16_f16 v[18:33], v[68:71], v[56:59], v[18:33]
	ds_read_b64_tr_b16 v[58:59], v45 offset:14464
	ds_read_b64_tr_b16 v[56:57], v45 offset:13888
	v_add_co_u32_e32 v68, vcc, s9, v38
	s_nop 1
	v_addc_co_u32_e32 v69, vcc, 0, v39, vcc
	v_add_co_u32_e32 v70, vcc, s9, v40
	s_waitcnt vmcnt(7) lgkmcnt(2)
	v_mfma_f32_32x32x16_f16 v[2:17], v[72:75], v[52:55], v[2:17]
	v_addc_co_u32_e32 v71, vcc, 0, v41, vcc
	ds_read_b64_tr_b16 v[52:53], v45 offset:16128
	ds_read_b64_tr_b16 v[54:55], v45 offset:16704
	v_add_co_u32_e32 v106, vcc, s8, v36
	s_mov_b32 s8, 0x300000
	s_nop 0
	v_addc_co_u32_e32 v107, vcc, 0, v37, vcc
	s_waitcnt lgkmcnt(2)
	v_mfma_f32_32x32x16_f16 v[18:33], v[72:75], v[56:59], v[18:33]
	global_load_dwordx4 v[56:59], v[68:69], off
	global_load_dwordx4 v[60:63], v[70:71], off
	ds_read_b64_tr_b16 v[70:71], v45 offset:16768
	ds_read_b64_tr_b16 v[68:69], v45 offset:16192
	s_mov_b32 s9, 0x380000
	s_waitcnt vmcnt(8) lgkmcnt(2)
	v_mfma_f32_32x32x16_f16 v[2:17], v[76:79], v[52:55], v[2:17]
	global_load_dwordx4 v[52:55], v[106:107], off offset:-4096
	global_load_dwordx4 v[72:75], v[104:105], off offset:1024
	global_load_dwordx4 v[84:87], v[104:105], off offset:2048
	global_load_dwordx4 v[100:103], v[104:105], off offset:3072
	s_waitcnt vmcnt(9)
	ds_write_b128 v46, v[64:67]
	s_waitcnt vmcnt(8)
	ds_write_b128 v34, v[88:91]
	s_waitcnt lgkmcnt(2)
	v_mfma_f32_32x32x16_f16 v[18:33], v[76:79], v[68:71], v[18:33]
	s_waitcnt lgkmcnt(0)
	s_barrier
	ds_read_b64_tr_b16 v[64:65], v45
	ds_read_b64_tr_b16 v[66:67], v45 offset:576
	ds_read_b64_tr_b16 v[70:71], v45 offset:640
	ds_read_b64_tr_b16 v[68:69], v45 offset:64
	v_add_co_u32_e32 v104, vcc, s8, v38
	s_waitcnt lgkmcnt(2)
	v_mfma_f32_32x32x16_f16 v[2:17], v[48:51], v[64:67], v[2:17]
	v_addc_co_u32_e32 v105, vcc, 0, v39, vcc
	v_add_co_u32_e32 v108, vcc, s8, v40
	s_movk_i32 s8, 0x7000
	s_nop 0
	v_addc_co_u32_e32 v109, vcc, 0, v41, vcc
	s_waitcnt lgkmcnt(0)
	v_mfma_f32_32x32x16_f16 v[18:33], v[48:51], v[68:71], v[18:33]
	ds_read_b64_tr_b16 v[48:49], v45 offset:2304
	ds_read_b64_tr_b16 v[50:51], v45 offset:2880
	ds_read_b64_tr_b16 v[66:67], v45 offset:2944
	ds_read_b64_tr_b16 v[64:65], v45 offset:2368
	s_waitcnt lgkmcnt(2)
	v_mfma_f32_32x32x16_f16 v[2:17], v[80:83], v[48:51], v[2:17]
	s_waitcnt lgkmcnt(0)
	v_mfma_f32_32x32x16_f16 v[18:33], v[80:83], v[64:67], v[18:33]
	ds_read_b64_tr_b16 v[48:49], v45 offset:4608
	ds_read_b64_tr_b16 v[50:51], v45 offset:5184
	ds_read_b64_tr_b16 v[66:67], v45 offset:5248
	ds_read_b64_tr_b16 v[64:65], v45 offset:4672
	s_waitcnt vmcnt(7) lgkmcnt(2)
	v_mfma_f32_32x32x16_f16 v[2:17], v[92:95], v[48:51], v[2:17]
	ds_read_b64_tr_b16 v[48:49], v45 offset:6912
	ds_read_b64_tr_b16 v[50:51], v45 offset:7488
	s_waitcnt lgkmcnt(2)
	v_mfma_f32_32x32x16_f16 v[18:33], v[92:95], v[64:67], v[18:33]
	ds_read_b64_tr_b16 v[66:67], v45 offset:7552
	ds_read_b64_tr_b16 v[64:65], v45 offset:6976
	s_waitcnt vmcnt(6) lgkmcnt(2)
	v_mfma_f32_32x32x16_f16 v[2:17], v[96:99], v[48:51], v[2:17]
	global_load_dwordx4 v[48:51], v[104:105], off
	global_load_dwordx4 v[68:71], v[108:109], off
	global_load_dwordx4 v[76:79], v[106:107], off
	global_load_dwordx4 v[80:83], v[106:107], off offset:1024
	global_load_dwordx4 v[88:91], v[106:107], off offset:2048
	global_load_dwordx4 v[92:95], v[106:107], off offset:3072
	s_waitcnt vmcnt(11)
	ds_write_b128 v46, v[56:59] offset:9216
	s_waitcnt vmcnt(10)
	ds_write_b128 v34, v[60:63] offset:9216
	s_waitcnt lgkmcnt(0)
	s_barrier
	ds_read_b64_tr_b16 v[56:57], v45 offset:9216
	ds_read_b64_tr_b16 v[58:59], v45 offset:9792
	ds_read_b64_tr_b16 v[62:63], v45 offset:9856
	ds_read_b64_tr_b16 v[60:61], v45 offset:9280
	v_mfma_f32_32x32x16_f16 v[18:33], v[96:99], v[64:67], v[18:33]
	s_waitcnt vmcnt(9) lgkmcnt(2)
	v_mfma_f32_32x32x16_f16 v[2:17], v[52:55], v[56:59], v[2:17]
	s_waitcnt lgkmcnt(0)
	v_mfma_f32_32x32x16_f16 v[18:33], v[52:55], v[60:63], v[18:33]
	ds_read_b64_tr_b16 v[52:53], v45 offset:11520
	ds_read_b64_tr_b16 v[54:55], v45 offset:12096
	ds_read_b64_tr_b16 v[58:59], v45 offset:12160
	ds_read_b64_tr_b16 v[56:57], v45 offset:11584
	v_add_co_u32_e32 v60, vcc, s9, v38
	s_nop 1
	v_addc_co_u32_e32 v61, vcc, 0, v39, vcc
	v_add_co_u32_e32 v62, vcc, s9, v40
	s_waitcnt vmcnt(8) lgkmcnt(2)
	v_mfma_f32_32x32x16_f16 v[2:17], v[72:75], v[52:55], v[2:17]
	ds_read_b64_tr_b16 v[52:53], v45 offset:13824
	ds_read_b64_tr_b16 v[54:55], v45 offset:14400
	v_addc_co_u32_e32 v63, vcc, 0, v41, vcc
	v_add_co_u32_e32 v36, vcc, s8, v36
	s_movk_i32 s8, 0x110
	s_nop 0
	v_addc_co_u32_e32 v37, vcc, 0, v37, vcc
	s_waitcnt lgkmcnt(2)
	v_mfma_f32_32x32x16_f16 v[18:33], v[72:75], v[56:59], v[18:33]
	ds_read_b64_tr_b16 v[58:59], v45 offset:14464
	ds_read_b64_tr_b16 v[56:57], v45 offset:13888
	s_waitcnt vmcnt(7) lgkmcnt(2)
	v_mfma_f32_32x32x16_f16 v[2:17], v[84:87], v[52:55], v[2:17]
	global_load_dwordx4 v[38:41], v[60:61], off
	global_load_dwordx4 v[52:55], v[62:63], off
	s_waitcnt lgkmcnt(0)
	v_mfma_f32_32x32x16_f16 v[18:33], v[84:87], v[56:59], v[18:33]
	ds_read_b64_tr_b16 v[56:57], v45 offset:16128
	ds_read_b64_tr_b16 v[58:59], v45 offset:16704
	global_load_dwordx4 v[60:63], v[36:37], off
	ds_read_b64_tr_b16 v[66:67], v45 offset:16768
	ds_read_b64_tr_b16 v[64:65], v45 offset:16192
	s_waitcnt vmcnt(9) lgkmcnt(2)
	v_mfma_f32_32x32x16_f16 v[2:17], v[100:103], v[56:59], v[2:17]
	global_load_dwordx4 v[56:59], v[36:37], off offset:1024
	global_load_dwordx4 v[72:75], v[36:37], off offset:2048
	global_load_dwordx4 v[84:87], v[36:37], off offset:3072
	s_waitcnt vmcnt(11)
	ds_write_b128 v46, v[48:51]
	s_waitcnt vmcnt(10)
	ds_write_b128 v34, v[68:71]
	s_waitcnt lgkmcnt(2)
	v_mfma_f32_32x32x16_f16 v[18:33], v[100:103], v[64:67], v[18:33]
	s_waitcnt lgkmcnt(0)
	s_barrier
	ds_read_b64_tr_b16 v[48:49], v45
	ds_read_b64_tr_b16 v[50:51], v45 offset:576
	ds_read_b64_tr_b16 v[66:67], v45 offset:640
	ds_read_b64_tr_b16 v[64:65], v45 offset:64
	s_waitcnt vmcnt(9) lgkmcnt(2)
	v_mfma_f32_32x32x16_f16 v[2:17], v[76:79], v[48:51], v[2:17]
	s_waitcnt lgkmcnt(0)
	v_mfma_f32_32x32x16_f16 v[18:33], v[76:79], v[64:67], v[18:33]
	ds_read_b64_tr_b16 v[48:49], v45 offset:2304
	ds_read_b64_tr_b16 v[50:51], v45 offset:2880
	ds_read_b64_tr_b16 v[66:67], v45 offset:2944
	ds_read_b64_tr_b16 v[64:65], v45 offset:2368
	s_waitcnt vmcnt(8) lgkmcnt(2)
	v_mfma_f32_32x32x16_f16 v[2:17], v[80:83], v[48:51], v[2:17]
	s_waitcnt lgkmcnt(0)
	v_mfma_f32_32x32x16_f16 v[18:33], v[80:83], v[64:67], v[18:33]
	ds_read_b64_tr_b16 v[48:49], v45 offset:4608
	ds_read_b64_tr_b16 v[50:51], v45 offset:5184
	ds_read_b64_tr_b16 v[66:67], v45 offset:5248
	ds_read_b64_tr_b16 v[64:65], v45 offset:4672
	s_waitcnt vmcnt(7) lgkmcnt(2)
	v_mfma_f32_32x32x16_f16 v[2:17], v[88:91], v[48:51], v[2:17]
	s_waitcnt lgkmcnt(0)
	v_mfma_f32_32x32x16_f16 v[18:33], v[88:91], v[64:67], v[18:33]
	ds_read_b64_tr_b16 v[48:49], v45 offset:6912
	ds_read_b64_tr_b16 v[50:51], v45 offset:7488
	ds_read_b64_tr_b16 v[66:67], v45 offset:7552
	ds_read_b64_tr_b16 v[64:65], v45 offset:6976
	s_waitcnt vmcnt(5)
	ds_write_b128 v46, v[38:41] offset:9216
	s_waitcnt vmcnt(4)
	ds_write_b128 v34, v[52:55] offset:9216
	s_waitcnt lgkmcnt(0)
	s_barrier
	v_mfma_f32_32x32x16_f16 v[2:17], v[92:95], v[48:51], v[2:17]
	ds_read_b64_tr_b16 v[36:37], v45 offset:9216
	ds_read_b64_tr_b16 v[38:39], v45 offset:9792
	ds_read_b64_tr_b16 v[48:49], v45 offset:9856
	ds_read_b64_tr_b16 v[46:47], v45 offset:9280
	v_and_b32_e32 v34, 4, v44
	v_lshl_or_b32 v34, v43, 5, v34
	v_mul_u32_u24_e32 v34, 0x110, v34
	v_mfma_f32_32x32x16_f16 v[18:33], v[92:95], v[64:67], v[18:33]
	s_waitcnt vmcnt(3) lgkmcnt(2)
	v_mfma_f32_32x32x16_f16 v[2:17], v[60:63], v[36:39], v[2:17]
	s_waitcnt lgkmcnt(0)
	v_mfma_f32_32x32x16_f16 v[18:33], v[60:63], v[46:49], v[18:33]
	ds_read_b64_tr_b16 v[36:37], v45 offset:11520
	ds_read_b64_tr_b16 v[38:39], v45 offset:12096
	ds_read_b64_tr_b16 v[48:49], v45 offset:12160
	ds_read_b64_tr_b16 v[46:47], v45 offset:11584
	s_waitcnt vmcnt(2) lgkmcnt(2)
	v_mfma_f32_32x32x16_f16 v[2:17], v[56:59], v[36:39], v[2:17]
	s_waitcnt lgkmcnt(0)
	v_mfma_f32_32x32x16_f16 v[18:33], v[56:59], v[46:49], v[18:33]
	ds_read_b64_tr_b16 v[36:37], v45 offset:13824
	ds_read_b64_tr_b16 v[38:39], v45 offset:14400
	ds_read_b64_tr_b16 v[48:49], v45 offset:14464
	ds_read_b64_tr_b16 v[46:47], v45 offset:13888
	s_waitcnt vmcnt(1) lgkmcnt(2)
	v_mfma_f32_32x32x16_f16 v[2:17], v[72:75], v[36:39], v[2:17]
	s_waitcnt lgkmcnt(0)
	v_mfma_f32_32x32x16_f16 v[18:33], v[72:75], v[46:49], v[18:33]
	ds_read_b64_tr_b16 v[36:37], v45 offset:16128
	ds_read_b64_tr_b16 v[38:39], v45 offset:16704
	ds_read_b64_tr_b16 v[48:49], v45 offset:16768
	ds_read_b64_tr_b16 v[46:47], v45 offset:16192
	s_waitcnt lgkmcnt(0)
	s_barrier
	s_waitcnt vmcnt(0)
	v_mfma_f32_32x32x16_f16 v[2:17], v[84:87], v[36:39], v[2:17]
	v_and_b32_e32 v36, 31, v0
	v_lshl_add_u32 v34, v36, 2, v34
	v_mfma_f32_32x32x16_f16 v[18:33], v[84:87], v[46:49], v[18:33]
	s_nop 11
	ds_write2_b32 v34, v2, v18 offset1:32
	ds_write2_b32 v34, v3, v19 offset0:68 offset1:100
	ds_write2_b32 v34, v4, v20 offset0:136 offset1:168
	ds_write2_b32 v34, v5, v21 offset0:204 offset1:236
	v_add_u32_e32 v2, 0x800, v34
	ds_write2_b32 v2, v6, v22 offset0:32 offset1:64
	ds_write2_b32 v2, v7, v23 offset0:100 offset1:132
	ds_write2_b32 v2, v8, v24 offset0:168 offset1:200
	v_add_u32_e32 v2, 0xa00, v34
	ds_write2_b32 v2, v9, v25 offset0:108 offset1:140
	v_add_u32_e32 v2, 0x1000, v34
	ds_write2_b32 v2, v10, v26 offset0:64 offset1:96
	ds_write2_b32 v2, v11, v27 offset0:132 offset1:164
	ds_write2_b32 v2, v12, v28 offset0:200 offset1:232
	v_add_u32_e32 v2, 0x1400, v34
	ds_write2_b32 v2, v13, v29 offset0:12 offset1:44
	v_add_u32_e32 v2, 0x1800, v34
	v_lshrrev_b32_e32 v4, 4, v0
	ds_write2_b32 v2, v14, v30 offset0:96 offset1:128
	ds_write2_b32 v2, v15, v31 offset0:164 offset1:196
	v_add_u32_e32 v2, 0x1a00, v34
	v_or_b32_e32 v10, s3, v4
	ds_write2_b32 v2, v16, v32 offset0:104 offset1:136
	v_add_u32_e32 v2, 0x1c00, v34
	v_ashrrev_i32_e32 v11, 31, v10
	ds_write2_b32 v2, v17, v33 offset0:44 offset1:76
	v_lshl_add_u64 v[2:3], v[10:11], 2, s[4:5]
	s_waitcnt lgkmcnt(0)
	s_barrier
	v_and_b32_e32 v34, 0xf0, v42
	s_movk_i32 s8, 0x110
	v_mad_u32_u24 v6, v4, s8, v34
	ds_read_b128 v[60:63], v6
	ds_read_b128 v[64:67], v6 offset:4352
	ds_read_b128 v[68:71], v6 offset:8704
	ds_read_b128 v[72:75], v6 offset:13056
	ds_read_b128 v[76:79], v6 offset:17408
	ds_read_b128 v[80:83], v6 offset:21760
	ds_read_b128 v[84:87], v6 offset:26112
	ds_read_b128 v[88:91], v6 offset:30464
	v_mov_b32_e32 v11, 0
	v_lshl_add_u64 v[14:15], s[0:1], 0, v[34:35]
	v_lshlrev_b64 v[12:13], 14, v[10:11]
	v_lshl_add_u64 v[12:13], v[14:15], 0, v[12:13]
	s_mov_b32 s10, 0x40000
	s_mov_b32 s11, 0
	s_waitcnt vmcnt(0)
	s_waitcnt lgkmcnt(7)
	v_pk_add_f32 v[60:61], v[60:61], v[110:111] op_sel_hi:[1,0]
	v_pk_add_f32 v[62:63], v[62:63], v[110:111] op_sel_hi:[1,0]
	global_store_dwordx4 v[12:13], v[60:63], off nt
	v_lshl_add_u64 v[12:13], v[12:13], 0, s[10:11]
	s_waitcnt lgkmcnt(6)
	v_pk_add_f32 v[64:65], v[64:65], v[112:113] op_sel_hi:[1,0]
	v_pk_add_f32 v[66:67], v[66:67], v[112:113] op_sel_hi:[1,0]
	global_store_dwordx4 v[12:13], v[64:67], off nt
	v_lshl_add_u64 v[12:13], v[12:13], 0, s[10:11]
	s_waitcnt lgkmcnt(5)
	v_pk_add_f32 v[68:69], v[68:69], v[114:115] op_sel_hi:[1,0]
	v_pk_add_f32 v[70:71], v[70:71], v[114:115] op_sel_hi:[1,0]
	global_store_dwordx4 v[12:13], v[68:71], off nt
	v_lshl_add_u64 v[12:13], v[12:13], 0, s[10:11]
	s_waitcnt lgkmcnt(4)
	v_pk_add_f32 v[72:73], v[72:73], v[116:117] op_sel_hi:[1,0]
	v_pk_add_f32 v[74:75], v[74:75], v[116:117] op_sel_hi:[1,0]
	global_store_dwordx4 v[12:13], v[72:75], off nt
	v_lshl_add_u64 v[12:13], v[12:13], 0, s[10:11]
	s_waitcnt lgkmcnt(3)
	v_pk_add_f32 v[76:77], v[76:77], v[118:119] op_sel_hi:[1,0]
	v_pk_add_f32 v[78:79], v[78:79], v[118:119] op_sel_hi:[1,0]
	global_store_dwordx4 v[12:13], v[76:79], off nt
	v_lshl_add_u64 v[12:13], v[12:13], 0, s[10:11]
	s_waitcnt lgkmcnt(2)
	v_pk_add_f32 v[80:81], v[80:81], v[120:121] op_sel_hi:[1,0]
	v_pk_add_f32 v[82:83], v[82:83], v[120:121] op_sel_hi:[1,0]
	global_store_dwordx4 v[12:13], v[80:83], off nt
	v_lshl_add_u64 v[12:13], v[12:13], 0, s[10:11]
	s_waitcnt lgkmcnt(1)
	v_pk_add_f32 v[84:85], v[84:85], v[122:123] op_sel_hi:[1,0]
	v_pk_add_f32 v[86:87], v[86:87], v[122:123] op_sel_hi:[1,0]
	global_store_dwordx4 v[12:13], v[84:87], off nt
	v_lshl_add_u64 v[12:13], v[12:13], 0, s[10:11]
	s_waitcnt lgkmcnt(0)
	v_pk_add_f32 v[88:89], v[88:89], v[124:125] op_sel_hi:[1,0]
	v_pk_add_f32 v[90:91], v[90:91], v[124:125] op_sel_hi:[1,0]
	global_store_dwordx4 v[12:13], v[88:91], off nt
	s_endpgm
	.p2alignl 8, 3212836864

	.amdhsa_kernel _Z9k_gemm_tlILi3ELb0EEvPKDF16_6TlArgs
		.amdhsa_group_segment_fixed_size 34816
		.amdhsa_private_segment_fixed_size 0
		.amdhsa_kernarg_size 80
		.amdhsa_user_sgpr_count 2
		.amdhsa_user_sgpr_dispatch_ptr 0
		.amdhsa_user_sgpr_queue_ptr 0
		.amdhsa_user_sgpr_kernarg_segment_ptr 1
		.amdhsa_user_sgpr_dispatch_id 0
		.amdhsa_user_sgpr_kernarg_preload_length 0
		.amdhsa_user_sgpr_kernarg_preload_offset 0
		.amdhsa_user_sgpr_private_segment_size 0
		.amdhsa_uses_dynamic_stack 0
		.amdhsa_enable_private_segment 0
		.amdhsa_system_sgpr_workgroup_id_x 1
		.amdhsa_system_sgpr_workgroup_id_y 1
		.amdhsa_system_sgpr_workgroup_id_z 0
		.amdhsa_system_sgpr_workgroup_info 0
		.amdhsa_system_vgpr_workitem_id 0
		.amdhsa_next_free_vgpr 169
		.amdhsa_next_free_sgpr 96
		.amdhsa_accum_offset 128
		.amdhsa_reserve_vcc 1
		.amdhsa_float_round_mode_32 0
		.amdhsa_float_round_mode_16_64 0
		.amdhsa_float_denorm_mode_32 3
		.amdhsa_float_denorm_mode_16_64 3
		.amdhsa_dx10_clamp 1
		.amdhsa_ieee_mode 1
		.amdhsa_fp16_overflow 0
		.amdhsa_tg_split 0
		.amdhsa_exception_fp_ieee_invalid_op 0
		.amdhsa_exception_fp_denorm_src 0
		.amdhsa_exception_fp_ieee_div_zero 0
		.amdhsa_exception_fp_ieee_overflow 0
		.amdhsa_exception_fp_ieee_underflow 0
		.amdhsa_exception_fp_ieee_inexact 0
		.amdhsa_exception_int_div_zero 0
	.end_amdhsa_kernel

amdhsa.kernels:
  - .agpr_count:     0
    .args:
      - .actual_access:  read_only
        .address_space:  global
        .offset:         0
        .size:           8
        .value_kind:     global_buffer
      - .actual_access:  read_only
        .address_space:  global
        .offset:         8
        .size:           8
        .value_kind:     global_buffer
      - .actual_access:  read_only
        .address_space:  global
        .offset:         16
        .size:           8
        .value_kind:     global_buffer
      - .actual_access:  write_only
        .address_space:  global
        .offset:         24
        .size:           8
        .value_kind:     global_buffer
      - .actual_access:  write_only
        .address_space:  global
        .offset:         32
        .size:           8
        .value_kind:     global_buffer
      - .actual_access:  write_only
        .address_space:  global
        .offset:         40
        .size:           8
        .value_kind:     global_buffer
      - .offset:         48
        .size:           104
        .value_kind:     by_value
    .group_segment_fixed_size: 37248
    .kernarg_segment_align: 8
    .kernarg_segment_size: 152
    .language:       OpenCL C
    .language_version:
      - 2
      - 0
    .max_flat_workgroup_size: 512
    .name:           _Z4k_lnPKfS0_S0_PDF16_PfS2_7CvtArgs
    .private_segment_fixed_size: 0
    .sgpr_count:     40
    .sgpr_spill_count: 0
    .symbol:         _Z4k_lnPKfS0_S0_PDF16_PfS2_7CvtArgs.kd
    .uniform_work_group_size: 1
    .uses_dynamic_stack: false
    .vgpr_count:     118
    .vgpr_spill_count: 0
    .wavefront_size: 64
  - .agpr_count:     36
    .args:
      - .actual_access:  read_only
        .address_space:  global
        .offset:         0
        .size:           8
        .value_kind:     global_buffer
      - .actual_access:  read_only
        .address_space:  global
        .offset:         8
        .size:           8
        .value_kind:     global_buffer
      - .actual_access:  read_only
        .address_space:  global
        .offset:         16
        .size:           8
        .value_kind:     global_buffer
      - .actual_access:  read_only
        .address_space:  global
        .offset:         24
        .size:           8
        .value_kind:     global_buffer
      - .actual_access:  read_only
        .address_space:  global
        .offset:         32
        .size:           8
        .value_kind:     global_buffer
      - .actual_access:  read_only
        .address_space:  global
        .offset:         40
        .size:           8
        .value_kind:     global_buffer
      - .actual_access:  read_only
        .address_space:  global
        .offset:         48
        .size:           8
        .value_kind:     global_buffer
      - .actual_access:  read_only
        .address_space:  global
        .offset:         56
        .size:           8
        .value_kind:     global_buffer
      - .actual_access:  write_only
        .address_space:  global
        .offset:         64
        .size:           8
        .value_kind:     global_buffer
      - .actual_access:  write_only
        .address_space:  global
        .offset:         72
        .size:           8
        .value_kind:     global_buffer
      - .actual_access:  write_only
        .address_space:  global
        .offset:         80
        .size:           8
        .value_kind:     global_buffer
      - .actual_access:  write_only
        .address_space:  global
        .offset:         88
        .size:           8
        .value_kind:     global_buffer
      - .actual_access:  write_only
        .address_space:  global
        .offset:         96
        .size:           8
        .value_kind:     global_buffer
    .group_segment_fixed_size: 77312
    .kernarg_segment_align: 8
    .kernarg_segment_size: 104
    .language:       OpenCL C
    .language_version:
      - 2
      - 0
    .max_flat_workgroup_size: 256
    .name:           _Z7k_frontPKDF16_S0_PKfS2_S0_S2_S2_S2_PjPfS4_S4_S4_
    .private_segment_fixed_size: 0
    .sgpr_count:     25
    .sgpr_spill_count: 0
    .symbol:         _Z7k_frontPKDF16_S0_PKfS2_S0_S2_S2_S2_PjPfS4_S4_S4_.kd
    .uniform_work_group_size: 1
    .uses_dynamic_stack: false
    .vgpr_count:     204
    .vgpr_spill_count: 0
    .wavefront_size: 64
  - .agpr_count:     0
    .args:
      - .actual_access:  read_only
        .address_space:  global
        .offset:         0
        .size:           8
        .value_kind:     global_buffer
      - .address_space:  global
        .offset:         8
        .size:           8
        .value_kind:     global_buffer
      - .actual_access:  read_only
        .address_space:  global
        .offset:         16
        .size:           8
        .value_kind:     global_buffer
    .group_segment_fixed_size: 0
    .kernarg_segment_align: 8
    .kernarg_segment_size: 24
    .language:       OpenCL C
    .language_version:
      - 2
      - 0
    .max_flat_workgroup_size: 64
    .name:           _Z7k_scan2PKfPfS0_
    .private_segment_fixed_size: 0
    .sgpr_count:     48
    .sgpr_spill_count: 0
    .symbol:         _Z7k_scan2PKfPfS0_.kd
    .uniform_work_group_size: 1
    .uses_dynamic_stack: false
    .vgpr_count:     150
    .vgpr_spill_count: 0
    .wavefront_size: 64
  - .agpr_count:     0
    .args:
      - .actual_access:  read_only
        .address_space:  global
        .offset:         0
        .size:           8
        .value_kind:     global_buffer
      - .actual_access:  read_only
        .address_space:  global
        .offset:         8
        .size:           8
        .value_kind:     global_buffer
      - .actual_access:  read_only
        .address_space:  global
        .offset:         16
        .size:           8
        .value_kind:     global_buffer
      - .actual_access:  read_only
        .address_space:  global
        .offset:         24
        .size:           8
        .value_kind:     global_buffer
      - .actual_access:  read_only
        .address_space:  global
        .offset:         32
        .size:           8
        .value_kind:     global_buffer
      - .actual_access:  read_only
        .address_space:  global
        .offset:         40
        .size:           8
        .value_kind:     global_buffer
      - .actual_access:  read_only
        .address_space:  global
        .offset:         48
        .size:           8
        .value_kind:     global_buffer
      - .actual_access:  read_only
        .address_space:  global
        .offset:         56
        .size:           8
        .value_kind:     global_buffer
      - .actual_access:  read_only
        .address_space:  global
        .offset:         64
        .size:           8
        .value_kind:     global_buffer
      - .offset:         72
        .size:           72
        .value_kind:     by_value
    .group_segment_fixed_size: 60416
    .kernarg_segment_align: 8
    .kernarg_segment_size: 144
    .language:       OpenCL C
    .language_version:
      - 2
      - 0
    .max_flat_workgroup_size: 256
    .name:           _Z7k_scan3PKjPKfS2_S2_S2_S2_PKDF16_S4_S4_7EpiArgs
    .private_segment_fixed_size: 0
    .sgpr_count:     34
    .sgpr_spill_count: 0
    .symbol:         _Z7k_scan3PKjPKfS2_S2_S2_S2_PKDF16_S4_S4_7EpiArgs.kd
    .uniform_work_group_size: 1
    .uses_dynamic_stack: false
    .vgpr_count:     236
    .vgpr_spill_count: 0
    .wavefront_size: 64
  - .agpr_count:     0
    .args:
      - .actual_access:  read_only
        .address_space:  global
        .offset:         0
        .size:           8
        .value_kind:     global_buffer
      - .actual_access:  read_only
        .address_space:  global
        .offset:         8
        .size:           8
        .value_kind:     global_buffer
      - .actual_access:  read_only
        .address_space:  global
        .offset:         16
        .size:           8
        .value_kind:     global_buffer
      - .actual_access:  write_only
        .address_space:  global
        .offset:         24
        .size:           8
        .value_kind:     global_buffer
    .group_segment_fixed_size: 20160
    .kernarg_segment_align: 8
    .kernarg_segment_size: 32
    .language:       OpenCL C
    .language_version:
      - 2
      - 0
    .max_flat_workgroup_size: 256
    .name:           _Z8k_dwconvPKDF16_PKfS2_PDF16_
    .private_segment_fixed_size: 0
    .sgpr_count:     86
    .sgpr_spill_count: 0
    .symbol:         _Z8k_dwconvPKDF16_PKfS2_PDF16_.kd
    .uniform_work_group_size: 1
    .uses_dynamic_stack: false
    .vgpr_count:     65
    .vgpr_spill_count: 0
    .wavefront_size: 64
  - .agpr_count:     0
    .args:
      - .actual_access:  read_only
        .address_space:  global
        .offset:         0
        .size:           8
        .value_kind:     global_buffer
      - .offset:         8
        .size:           72
        .value_kind:     by_value
    .group_segment_fixed_size: 38912
    .kernarg_segment_align: 8
    .kernarg_segment_size: 80
    .language:       OpenCL C
    .language_version:
      - 2
      - 0
    .max_flat_workgroup_size: 256
    .name:           _Z9k_gemm_tlILi2ELb1EEvPKDF16_6TlArgs
    .private_segment_fixed_size: 0
    .sgpr_count:     27
    .sgpr_spill_count: 0
    .symbol:         _Z9k_gemm_tlILi2ELb1EEvPKDF16_6TlArgs.kd
    .uniform_work_group_size: 1
    .uses_dynamic_stack: false
    .vgpr_count:     124
    .vgpr_spill_count: 0
    .wavefront_size: 64
  - .agpr_count:     0
    .args:
      - .actual_access:  read_only
        .address_space:  global
        .offset:         0
        .size:           8
        .value_kind:     global_buffer
      - .offset:         8
        .size:           72
        .value_kind:     by_value
    .group_segment_fixed_size: 34816
    .kernarg_segment_align: 8
    .kernarg_segment_size: 80
    .language:       OpenCL C
    .language_version:
      - 2
      - 0
    .max_flat_workgroup_size: 256
    .name:           _Z9k_gemm_tlILi3ELb0EEvPKDF16_6TlArgs
    .private_segment_fixed_size: 0
    .sgpr_count:     18
    .sgpr_spill_count: 0
    .symbol:         _Z9k_gemm_tlILi3ELb0EEvPKDF16_6TlArgs.kd
    .uniform_work_group_size: 1
    .uses_dynamic_stack: false
    .vgpr_count:     127
    .vgpr_spill_count: 0
    .wavefront_size: 64
